# f27 plus attn fast path: accumulator zero-init v_movs dropped, first loop block accumulates onto a constant 0 (as the compiler's first iteration did)
# baseline (speedup 1.0000x reference)
.Lf_27:
	s_or_b64 exec, exec, s[2:3]
	v_and_b32_e32 v2, 0x3f0, v116
	v_add_u32_e32 v166, 0, v2
	s_waitcnt lgkmcnt(0)
	s_barrier
	s_mov_b32 s46, s8
	s_mov_b32 s47, s9
	global_load_dwordx4 v[66:69], v38, s[46:47]
	s_add_u32 s46, s46, 0x3000
	s_addc_u32 s47, s47, 0
	global_load_dwordx4 v[70:73], v38, s[46:47]
	s_add_u32 s46, s46, 0x3000
	s_addc_u32 s47, s47, 0
	global_load_dwordx4 v[74:77], v38, s[46:47]
	s_add_u32 s46, s46, 0x3000
	s_addc_u32 s47, s47, 0
	global_load_dwordx4 v[78:81], v38, s[46:47]
	v_and_b32_e32 v167, 31, v0
	v_lshl_or_b32 v167, s51, 5, v167
	s_mul_i32 s38, s33, 0x1800
	v_add_u32_e32 v2, s38, v167
	v_lshlrev_b32_e32 v2, 5, v2
	v_bfe_u32 v3, v0, 5, 1
	v_lshl_add_u32 v2, v3, 4, v2
	s_mov_b32 s44, s16
	s_mov_b32 s45, s17
	global_load_dwordx4 v[102:105], v2, s[44:45]
	s_add_u32 s44, s44, 0x3000
	s_addc_u32 s45, s45, 0
	global_load_dwordx4 v[106:109], v2, s[44:45]
	s_add_u32 s44, s44, 0x3000
	s_addc_u32 s45, s45, 0
	global_load_dwordx4 v[110:113], v2, s[44:45]
	s_add_u32 s44, s44, 0x3000
	s_addc_u32 s45, s45, 0
	global_load_dwordx4 v[114:117], v2, s[44:45]
	s_add_u32 s44, s44, 0x3000
	s_addc_u32 s45, s45, 0
	global_load_dwordx4 v[118:121], v2, s[44:45]
	s_add_u32 s44, s44, 0x3000
	s_addc_u32 s45, s45, 0
	global_load_dwordx4 v[122:125], v2, s[44:45]
	s_add_u32 s44, s44, 0x3000
	s_addc_u32 s45, s45, 0
	global_load_dwordx4 v[126:129], v2, s[44:45]
	s_add_u32 s44, s44, 0x3000
	s_addc_u32 s45, s45, 0
	global_load_dwordx4 v[130:133], v2, s[44:45]
	s_add_u32 s44, s44, 0x3000
	s_addc_u32 s45, s45, 0
	global_load_dwordx4 v[134:137], v2, s[44:45]
	s_add_u32 s44, s44, 0x3000
	s_addc_u32 s45, s45, 0
	global_load_dwordx4 v[138:141], v2, s[44:45]
	s_add_u32 s44, s44, 0x3000
	s_addc_u32 s45, s45, 0
	global_load_dwordx4 v[142:145], v2, s[44:45]
	s_add_u32 s44, s44, 0x3000
	s_addc_u32 s45, s45, 0
	global_load_dwordx4 v[146:149], v2, s[44:45]
	s_add_u32 s44, s44, 0x3000
	s_addc_u32 s45, s45, 0
	global_load_dwordx4 v[150:153], v2, s[44:45]
	s_add_u32 s44, s44, 0x3000
	s_addc_u32 s45, s45, 0
	global_load_dwordx4 v[154:157], v2, s[44:45]
	s_add_u32 s44, s44, 0x3000
	s_addc_u32 s45, s45, 0
	global_load_dwordx4 v[158:161], v2, s[44:45]
	s_add_u32 s44, s44, 0x3000
	s_addc_u32 s45, s45, 0
	global_load_dwordx4 v[162:165], v2, s[44:45]
	v_mul_u32_u24_e32 v1, 0xc80, v3
	v_lshl_add_u32 v1, v167, 1, v1
	v_add_u32_e32 v1, 0x18000, v1
	v_mov_b32_e32 v167, v39
	ds_read_b128 v[46:49], v166 offset:2048
	ds_read_b128 v[14:17], v166 offset:0
	ds_read_b128 v[30:33], v166 offset:1024
	ds_read_b128 v[62:65], v166 offset:3072
	s_waitcnt vmcnt(14) lgkmcnt(3)
	v_mfma_f32_32x32x16_f16 v[34:49], v[46:49], v[106:109], 0
	s_waitcnt lgkmcnt(2)
	v_mfma_f32_32x32x16_f16 v[2:17], v[14:17], v[102:105], 0
	s_waitcnt lgkmcnt(1)
	v_mfma_f32_32x32x16_f16 v[18:33], v[30:33], v[102:105], 0
	s_waitcnt lgkmcnt(0)
	v_mfma_f32_32x32x16_f16 v[50:65], v[62:65], v[106:109], 0
	ds_write_b128 v167, v[66:69]
	ds_write_b128 v167, v[70:73] offset:12800
	ds_write_b128 v167, v[74:77] offset:25600
	ds_write_b128 v167, v[78:81] offset:38400
	s_lshl_b32 s22, s42, 2
	s_cmpk_lt_u32 s49, 0x100
	s_cselect_b32 s20, s14, s10
	s_cselect_b32 s21, s15, s11
	s_cselect_b32 s22, s22, 0
	s_cselect_b32 s23, 0xff, 15
	v_and_b32_e32 v82, s23, v0
	v_lshlrev_b32_e32 v82, 4, v82
	v_add_u32_e32 v82, s22, v82
	global_load_dwordx4 v[102:105], v82, s[20:21]
	s_nop 7
	ds_read_b128 v[46:49], v166 offset:6144
	ds_read_b128 v[14:17], v166 offset:4096
	ds_read_b128 v[30:33], v166 offset:5120
	ds_read_b128 v[62:65], v166 offset:7168
	v_pk_mul_f32 v[66:67], v[34:35], v[18:19]
	v_pk_mul_f32 v[68:69], v[36:37], v[20:21]
	v_pk_mul_f32 v[70:71], v[38:39], v[22:23]
	v_pk_mul_f32 v[72:73], v[40:41], v[24:25]
	v_pk_mul_f32 v[74:75], v[42:43], v[26:27]
	v_pk_mul_f32 v[76:77], v[44:45], v[28:29]
	s_waitcnt vmcnt(13) lgkmcnt(3)
	v_mfma_f32_32x32x16_f16 v[34:49], v[46:49], v[114:117], 0
	v_pk_fma_f32 v[66:67], v[2:3], v[50:51], v[66:67]
	v_pk_fma_f32 v[68:69], v[4:5], v[52:53], v[68:69]
	v_pk_fma_f32 v[70:71], v[6:7], v[54:55], v[70:71]
	v_pk_fma_f32 v[72:73], v[8:9], v[56:57], v[72:73]
	v_pk_fma_f32 v[74:75], v[10:11], v[58:59], v[74:75]
	v_pk_fma_f32 v[76:77], v[12:13], v[60:61], v[76:77]
	s_waitcnt lgkmcnt(2)
	v_mfma_f32_32x32x16_f16 v[2:17], v[14:17], v[110:113], 0
	v_pk_mul_f32 v[78:79], v[18:19], v[50:51]
	v_pk_mul_f32 v[80:81], v[20:21], v[52:53]
	v_pk_mul_f32 v[82:83], v[22:23], v[54:55]
	v_pk_mul_f32 v[84:85], v[24:25], v[56:57]
	v_pk_mul_f32 v[86:87], v[26:27], v[58:59]
	v_pk_mul_f32 v[88:89], v[28:29], v[60:61]
	s_waitcnt lgkmcnt(1)
	v_mfma_f32_32x32x16_f16 v[18:33], v[30:33], v[110:113], 0
	s_waitcnt lgkmcnt(0)
	v_mfma_f32_32x32x16_f16 v[50:65], v[62:65], v[114:117], 0
	v_rcp_f32_e32 v78, v78
	v_rcp_f32_e32 v79, v79
	v_rcp_f32_e32 v80, v80
	v_rcp_f32_e32 v81, v81
	v_rcp_f32_e32 v82, v82
	v_rcp_f32_e32 v83, v83
	v_rcp_f32_e32 v84, v84
	v_rcp_f32_e32 v85, v85
	v_rcp_f32_e32 v86, v86
	v_rcp_f32_e32 v87, v87
	v_rcp_f32_e32 v88, v88
	v_rcp_f32_e32 v89, v89
	v_pk_fma_f32 v[90:91], v[66:67], v[78:79], 0 op_sel_hi:[1,1,0]
	v_pk_fma_f32 v[92:93], v[68:69], v[80:81], 0 op_sel_hi:[1,1,0]
	v_pk_fma_f32 v[94:95], v[70:71], v[82:83], 0 op_sel_hi:[1,1,0]
	v_pk_fma_f32 v[96:97], v[72:73], v[84:85], 0 op_sel_hi:[1,1,0]
	v_pk_fma_f32 v[98:99], v[74:75], v[86:87], 0 op_sel_hi:[1,1,0]
	v_pk_fma_f32 v[100:101], v[76:77], v[88:89], 0 op_sel_hi:[1,1,0]
	ds_read_b128 v[46:49], v166 offset:10240
	ds_read_b128 v[14:17], v166 offset:8192
	ds_read_b128 v[30:33], v166 offset:9216
	ds_read_b128 v[62:65], v166 offset:11264
	v_pk_mul_f32 v[66:67], v[34:35], v[18:19]
	v_pk_mul_f32 v[68:69], v[36:37], v[20:21]
	v_pk_mul_f32 v[70:71], v[38:39], v[22:23]
	v_pk_mul_f32 v[72:73], v[40:41], v[24:25]
	v_pk_mul_f32 v[74:75], v[42:43], v[26:27]
	v_pk_mul_f32 v[76:77], v[44:45], v[28:29]
	s_waitcnt vmcnt(11) lgkmcnt(3)
	v_mfma_f32_32x32x16_f16 v[34:49], v[46:49], v[122:125], 0
	v_pk_fma_f32 v[66:67], v[2:3], v[50:51], v[66:67]
	v_pk_fma_f32 v[68:69], v[4:5], v[52:53], v[68:69]
	v_pk_fma_f32 v[70:71], v[6:7], v[54:55], v[70:71]
	v_pk_fma_f32 v[72:73], v[8:9], v[56:57], v[72:73]
	v_pk_fma_f32 v[74:75], v[10:11], v[58:59], v[74:75]
	v_pk_fma_f32 v[76:77], v[12:13], v[60:61], v[76:77]
	s_waitcnt lgkmcnt(2)
	v_mfma_f32_32x32x16_f16 v[2:17], v[14:17], v[118:121], 0
	v_pk_mul_f32 v[78:79], v[18:19], v[50:51]
	v_pk_mul_f32 v[80:81], v[20:21], v[52:53]
	v_pk_mul_f32 v[82:83], v[22:23], v[54:55]
	v_pk_mul_f32 v[84:85], v[24:25], v[56:57]
	v_pk_mul_f32 v[86:87], v[26:27], v[58:59]
	v_pk_mul_f32 v[88:89], v[28:29], v[60:61]
	s_waitcnt lgkmcnt(1)
	v_mfma_f32_32x32x16_f16 v[18:33], v[30:33], v[118:121], 0
	s_waitcnt lgkmcnt(0)
	v_mfma_f32_32x32x16_f16 v[50:65], v[62:65], v[122:125], 0
	v_rcp_f32_e32 v78, v78
	v_rcp_f32_e32 v79, v79
	v_rcp_f32_e32 v80, v80
	v_rcp_f32_e32 v81, v81
	v_rcp_f32_e32 v82, v82
	v_rcp_f32_e32 v83, v83
	v_rcp_f32_e32 v84, v84
	v_rcp_f32_e32 v85, v85
	v_rcp_f32_e32 v86, v86
	v_rcp_f32_e32 v87, v87
	v_rcp_f32_e32 v88, v88
	v_rcp_f32_e32 v89, v89
	v_pk_fma_f32 v[90:91], v[66:67], v[78:79], v[90:91]
	v_pk_fma_f32 v[92:93], v[68:69], v[80:81], v[92:93]
	v_pk_fma_f32 v[94:95], v[70:71], v[82:83], v[94:95]
	v_pk_fma_f32 v[96:97], v[72:73], v[84:85], v[96:97]
	v_pk_fma_f32 v[98:99], v[74:75], v[86:87], v[98:99]
	v_pk_fma_f32 v[100:101], v[76:77], v[88:89], v[100:101]
	ds_read_b128 v[46:49], v166 offset:14336
	ds_read_b128 v[14:17], v166 offset:12288
	ds_read_b128 v[30:33], v166 offset:13312
	ds_read_b128 v[62:65], v166 offset:15360
	v_pk_mul_f32 v[66:67], v[34:35], v[18:19]
	v_pk_mul_f32 v[68:69], v[36:37], v[20:21]
	v_pk_mul_f32 v[70:71], v[38:39], v[22:23]
	v_pk_mul_f32 v[72:73], v[40:41], v[24:25]
	v_pk_mul_f32 v[74:75], v[42:43], v[26:27]
	v_pk_mul_f32 v[76:77], v[44:45], v[28:29]
	s_waitcnt vmcnt(9) lgkmcnt(3)
	v_mfma_f32_32x32x16_f16 v[34:49], v[46:49], v[130:133], 0
	v_pk_fma_f32 v[66:67], v[2:3], v[50:51], v[66:67]
	v_pk_fma_f32 v[68:69], v[4:5], v[52:53], v[68:69]
	v_pk_fma_f32 v[70:71], v[6:7], v[54:55], v[70:71]
	v_pk_fma_f32 v[72:73], v[8:9], v[56:57], v[72:73]
	v_pk_fma_f32 v[74:75], v[10:11], v[58:59], v[74:75]
	v_pk_fma_f32 v[76:77], v[12:13], v[60:61], v[76:77]
	s_waitcnt lgkmcnt(2)
	v_mfma_f32_32x32x16_f16 v[2:17], v[14:17], v[126:129], 0
	v_pk_mul_f32 v[78:79], v[18:19], v[50:51]
	v_pk_mul_f32 v[80:81], v[20:21], v[52:53]
	v_pk_mul_f32 v[82:83], v[22:23], v[54:55]
	v_pk_mul_f32 v[84:85], v[24:25], v[56:57]
	v_pk_mul_f32 v[86:87], v[26:27], v[58:59]
	v_pk_mul_f32 v[88:89], v[28:29], v[60:61]
	s_waitcnt lgkmcnt(1)
	v_mfma_f32_32x32x16_f16 v[18:33], v[30:33], v[126:129], 0
	s_waitcnt lgkmcnt(0)
	v_mfma_f32_32x32x16_f16 v[50:65], v[62:65], v[130:133], 0
	v_rcp_f32_e32 v78, v78
	v_rcp_f32_e32 v79, v79
	v_rcp_f32_e32 v80, v80
	v_rcp_f32_e32 v81, v81
	v_rcp_f32_e32 v82, v82
	v_rcp_f32_e32 v83, v83
	v_rcp_f32_e32 v84, v84
	v_rcp_f32_e32 v85, v85
	v_rcp_f32_e32 v86, v86
	v_rcp_f32_e32 v87, v87
	v_rcp_f32_e32 v88, v88
	v_rcp_f32_e32 v89, v89
	v_pk_fma_f32 v[90:91], v[66:67], v[78:79], v[90:91]
	v_pk_fma_f32 v[92:93], v[68:69], v[80:81], v[92:93]
	v_pk_fma_f32 v[94:95], v[70:71], v[82:83], v[94:95]
	v_pk_fma_f32 v[96:97], v[72:73], v[84:85], v[96:97]
	v_pk_fma_f32 v[98:99], v[74:75], v[86:87], v[98:99]
	v_pk_fma_f32 v[100:101], v[76:77], v[88:89], v[100:101]
	ds_read_b128 v[46:49], v166 offset:18432
	ds_read_b128 v[14:17], v166 offset:16384
	ds_read_b128 v[30:33], v166 offset:17408
	ds_read_b128 v[62:65], v166 offset:19456
	v_pk_mul_f32 v[66:67], v[34:35], v[18:19]
	v_pk_mul_f32 v[68:69], v[36:37], v[20:21]
	v_pk_mul_f32 v[70:71], v[38:39], v[22:23]
	v_pk_mul_f32 v[72:73], v[40:41], v[24:25]
	v_pk_mul_f32 v[74:75], v[42:43], v[26:27]
	v_pk_mul_f32 v[76:77], v[44:45], v[28:29]
	s_waitcnt vmcnt(7) lgkmcnt(3)
	v_mfma_f32_32x32x16_f16 v[34:49], v[46:49], v[138:141], 0
	v_pk_fma_f32 v[66:67], v[2:3], v[50:51], v[66:67]
	v_pk_fma_f32 v[68:69], v[4:5], v[52:53], v[68:69]
	v_pk_fma_f32 v[70:71], v[6:7], v[54:55], v[70:71]
	v_pk_fma_f32 v[72:73], v[8:9], v[56:57], v[72:73]
	v_pk_fma_f32 v[74:75], v[10:11], v[58:59], v[74:75]
	v_pk_fma_f32 v[76:77], v[12:13], v[60:61], v[76:77]
	s_waitcnt lgkmcnt(2)
	v_mfma_f32_32x32x16_f16 v[2:17], v[14:17], v[134:137], 0
	v_pk_mul_f32 v[78:79], v[18:19], v[50:51]
	v_pk_mul_f32 v[80:81], v[20:21], v[52:53]
	v_pk_mul_f32 v[82:83], v[22:23], v[54:55]
	v_pk_mul_f32 v[84:85], v[24:25], v[56:57]
	v_pk_mul_f32 v[86:87], v[26:27], v[58:59]
	v_pk_mul_f32 v[88:89], v[28:29], v[60:61]
	s_waitcnt lgkmcnt(1)
	v_mfma_f32_32x32x16_f16 v[18:33], v[30:33], v[134:137], 0
	s_waitcnt lgkmcnt(0)
	v_mfma_f32_32x32x16_f16 v[50:65], v[62:65], v[138:141], 0
	v_rcp_f32_e32 v78, v78
	v_rcp_f32_e32 v79, v79
	v_rcp_f32_e32 v80, v80
	v_rcp_f32_e32 v81, v81
	v_rcp_f32_e32 v82, v82
	v_rcp_f32_e32 v83, v83
	v_rcp_f32_e32 v84, v84
	v_rcp_f32_e32 v85, v85
	v_rcp_f32_e32 v86, v86
	v_rcp_f32_e32 v87, v87
	v_rcp_f32_e32 v88, v88
	v_rcp_f32_e32 v89, v89
	v_pk_fma_f32 v[90:91], v[66:67], v[78:79], v[90:91]
	v_pk_fma_f32 v[92:93], v[68:69], v[80:81], v[92:93]
	v_pk_fma_f32 v[94:95], v[70:71], v[82:83], v[94:95]
	v_pk_fma_f32 v[96:97], v[72:73], v[84:85], v[96:97]
	v_pk_fma_f32 v[98:99], v[74:75], v[86:87], v[98:99]
	v_pk_fma_f32 v[100:101], v[76:77], v[88:89], v[100:101]
	ds_read_b128 v[46:49], v166 offset:22528
	ds_read_b128 v[14:17], v166 offset:20480
	ds_read_b128 v[30:33], v166 offset:21504
	ds_read_b128 v[62:65], v166 offset:23552
	v_pk_mul_f32 v[66:67], v[34:35], v[18:19]
	v_pk_mul_f32 v[68:69], v[36:37], v[20:21]
	v_pk_mul_f32 v[70:71], v[38:39], v[22:23]
	v_pk_mul_f32 v[72:73], v[40:41], v[24:25]
	v_pk_mul_f32 v[74:75], v[42:43], v[26:27]
	v_pk_mul_f32 v[76:77], v[44:45], v[28:29]
	s_waitcnt vmcnt(5) lgkmcnt(3)
	v_mfma_f32_32x32x16_f16 v[34:49], v[46:49], v[146:149], 0
	v_pk_fma_f32 v[66:67], v[2:3], v[50:51], v[66:67]
	v_pk_fma_f32 v[68:69], v[4:5], v[52:53], v[68:69]
	v_pk_fma_f32 v[70:71], v[6:7], v[54:55], v[70:71]
	v_pk_fma_f32 v[72:73], v[8:9], v[56:57], v[72:73]
	v_pk_fma_f32 v[74:75], v[10:11], v[58:59], v[74:75]
	v_pk_fma_f32 v[76:77], v[12:13], v[60:61], v[76:77]
	s_waitcnt lgkmcnt(2)
	v_mfma_f32_32x32x16_f16 v[2:17], v[14:17], v[142:145], 0
	v_pk_mul_f32 v[78:79], v[18:19], v[50:51]
	v_pk_mul_f32 v[80:81], v[20:21], v[52:53]
	v_pk_mul_f32 v[82:83], v[22:23], v[54:55]
	v_pk_mul_f32 v[84:85], v[24:25], v[56:57]
	v_pk_mul_f32 v[86:87], v[26:27], v[58:59]
	v_pk_mul_f32 v[88:89], v[28:29], v[60:61]
	s_waitcnt lgkmcnt(1)
	v_mfma_f32_32x32x16_f16 v[18:33], v[30:33], v[142:145], 0
	s_waitcnt lgkmcnt(0)
	v_mfma_f32_32x32x16_f16 v[50:65], v[62:65], v[146:149], 0
	v_rcp_f32_e32 v78, v78
	v_rcp_f32_e32 v79, v79
	v_rcp_f32_e32 v80, v80
	v_rcp_f32_e32 v81, v81
	v_rcp_f32_e32 v82, v82
	v_rcp_f32_e32 v83, v83
	v_rcp_f32_e32 v84, v84
	v_rcp_f32_e32 v85, v85
	v_rcp_f32_e32 v86, v86
	v_rcp_f32_e32 v87, v87
	v_rcp_f32_e32 v88, v88
	v_rcp_f32_e32 v89, v89
	v_pk_fma_f32 v[90:91], v[66:67], v[78:79], v[90:91]
	v_pk_fma_f32 v[92:93], v[68:69], v[80:81], v[92:93]
	v_pk_fma_f32 v[94:95], v[70:71], v[82:83], v[94:95]
	v_pk_fma_f32 v[96:97], v[72:73], v[84:85], v[96:97]
	v_pk_fma_f32 v[98:99], v[74:75], v[86:87], v[98:99]
	v_pk_fma_f32 v[100:101], v[76:77], v[88:89], v[100:101]
	ds_read_b128 v[46:49], v166 offset:26624
	ds_read_b128 v[14:17], v166 offset:24576
	ds_read_b128 v[30:33], v166 offset:25600
	ds_read_b128 v[62:65], v166 offset:27648
	v_pk_mul_f32 v[66:67], v[34:35], v[18:19]
	v_pk_mul_f32 v[68:69], v[36:37], v[20:21]
	v_pk_mul_f32 v[70:71], v[38:39], v[22:23]
	v_pk_mul_f32 v[72:73], v[40:41], v[24:25]
	v_pk_mul_f32 v[74:75], v[42:43], v[26:27]
	v_pk_mul_f32 v[76:77], v[44:45], v[28:29]
	s_waitcnt vmcnt(3) lgkmcnt(3)
	v_mfma_f32_32x32x16_f16 v[34:49], v[46:49], v[154:157], 0
	v_pk_fma_f32 v[66:67], v[2:3], v[50:51], v[66:67]
	v_pk_fma_f32 v[68:69], v[4:5], v[52:53], v[68:69]
	v_pk_fma_f32 v[70:71], v[6:7], v[54:55], v[70:71]
	v_pk_fma_f32 v[72:73], v[8:9], v[56:57], v[72:73]
	v_pk_fma_f32 v[74:75], v[10:11], v[58:59], v[74:75]
	v_pk_fma_f32 v[76:77], v[12:13], v[60:61], v[76:77]
	s_waitcnt lgkmcnt(2)
	v_mfma_f32_32x32x16_f16 v[2:17], v[14:17], v[150:153], 0
	v_pk_mul_f32 v[78:79], v[18:19], v[50:51]
	v_pk_mul_f32 v[80:81], v[20:21], v[52:53]
	v_pk_mul_f32 v[82:83], v[22:23], v[54:55]
	v_pk_mul_f32 v[84:85], v[24:25], v[56:57]
	v_pk_mul_f32 v[86:87], v[26:27], v[58:59]
	v_pk_mul_f32 v[88:89], v[28:29], v[60:61]
	s_waitcnt lgkmcnt(1)
	v_mfma_f32_32x32x16_f16 v[18:33], v[30:33], v[150:153], 0
	s_waitcnt lgkmcnt(0)
	v_mfma_f32_32x32x16_f16 v[50:65], v[62:65], v[154:157], 0
	v_rcp_f32_e32 v78, v78
	v_rcp_f32_e32 v79, v79
	v_rcp_f32_e32 v80, v80
	v_rcp_f32_e32 v81, v81
	v_rcp_f32_e32 v82, v82
	v_rcp_f32_e32 v83, v83
	v_rcp_f32_e32 v84, v84
	v_rcp_f32_e32 v85, v85
	v_rcp_f32_e32 v86, v86
	v_rcp_f32_e32 v87, v87
	v_rcp_f32_e32 v88, v88
	v_rcp_f32_e32 v89, v89
	v_pk_fma_f32 v[90:91], v[66:67], v[78:79], v[90:91]
	v_pk_fma_f32 v[92:93], v[68:69], v[80:81], v[92:93]
	v_pk_fma_f32 v[94:95], v[70:71], v[82:83], v[94:95]
	v_pk_fma_f32 v[96:97], v[72:73], v[84:85], v[96:97]
	v_pk_fma_f32 v[98:99], v[74:75], v[86:87], v[98:99]
	v_pk_fma_f32 v[100:101], v[76:77], v[88:89], v[100:101]
	ds_read_b128 v[46:49], v166 offset:30720
	ds_read_b128 v[14:17], v166 offset:28672
	ds_read_b128 v[30:33], v166 offset:29696
	ds_read_b128 v[62:65], v166 offset:31744
	v_pk_mul_f32 v[66:67], v[34:35], v[18:19]
	v_pk_mul_f32 v[68:69], v[36:37], v[20:21]
	v_pk_mul_f32 v[70:71], v[38:39], v[22:23]
	v_pk_mul_f32 v[72:73], v[40:41], v[24:25]
	v_pk_mul_f32 v[74:75], v[42:43], v[26:27]
	v_pk_mul_f32 v[76:77], v[44:45], v[28:29]
	s_waitcnt vmcnt(1) lgkmcnt(3)
	v_mfma_f32_32x32x16_f16 v[34:49], v[46:49], v[162:165], 0
	v_pk_fma_f32 v[66:67], v[2:3], v[50:51], v[66:67]
	v_pk_fma_f32 v[68:69], v[4:5], v[52:53], v[68:69]
	v_pk_fma_f32 v[70:71], v[6:7], v[54:55], v[70:71]
	v_pk_fma_f32 v[72:73], v[8:9], v[56:57], v[72:73]
	v_pk_fma_f32 v[74:75], v[10:11], v[58:59], v[74:75]
	v_pk_fma_f32 v[76:77], v[12:13], v[60:61], v[76:77]
	s_waitcnt lgkmcnt(2)
	v_mfma_f32_32x32x16_f16 v[2:17], v[14:17], v[158:161], 0
	v_pk_mul_f32 v[78:79], v[18:19], v[50:51]
	v_pk_mul_f32 v[80:81], v[20:21], v[52:53]
	v_pk_mul_f32 v[82:83], v[22:23], v[54:55]
	v_pk_mul_f32 v[84:85], v[24:25], v[56:57]
	v_pk_mul_f32 v[86:87], v[26:27], v[58:59]
	v_pk_mul_f32 v[88:89], v[28:29], v[60:61]
	s_waitcnt lgkmcnt(1)
	v_mfma_f32_32x32x16_f16 v[18:33], v[30:33], v[158:161], 0
	s_waitcnt lgkmcnt(0)
	v_mfma_f32_32x32x16_f16 v[50:65], v[62:65], v[162:165], 0
	v_rcp_f32_e32 v78, v78
	v_rcp_f32_e32 v79, v79
	v_rcp_f32_e32 v80, v80
	v_rcp_f32_e32 v81, v81
	v_rcp_f32_e32 v82, v82
	v_rcp_f32_e32 v83, v83
	v_rcp_f32_e32 v84, v84
	v_rcp_f32_e32 v85, v85
	v_rcp_f32_e32 v86, v86
	v_rcp_f32_e32 v87, v87
	v_rcp_f32_e32 v88, v88
	v_rcp_f32_e32 v89, v89
	v_pk_fma_f32 v[90:91], v[66:67], v[78:79], v[90:91]
	v_pk_fma_f32 v[92:93], v[68:69], v[80:81], v[92:93]
	v_pk_fma_f32 v[94:95], v[70:71], v[82:83], v[94:95]
	v_pk_fma_f32 v[96:97], v[72:73], v[84:85], v[96:97]
	v_pk_fma_f32 v[98:99], v[74:75], v[86:87], v[98:99]
	v_pk_fma_f32 v[100:101], v[76:77], v[88:89], v[100:101]
	v_pk_mul_f32 v[66:67], v[34:35], v[18:19]
	v_pk_mul_f32 v[68:69], v[36:37], v[20:21]
	v_pk_mul_f32 v[70:71], v[38:39], v[22:23]
	v_pk_mul_f32 v[72:73], v[40:41], v[24:25]
	v_pk_mul_f32 v[74:75], v[42:43], v[26:27]
	v_pk_mul_f32 v[76:77], v[44:45], v[28:29]
	v_pk_fma_f32 v[66:67], v[2:3], v[50:51], v[66:67]
	v_pk_fma_f32 v[68:69], v[4:5], v[52:53], v[68:69]
	v_pk_fma_f32 v[70:71], v[6:7], v[54:55], v[70:71]
	v_pk_fma_f32 v[72:73], v[8:9], v[56:57], v[72:73]
	v_pk_fma_f32 v[74:75], v[10:11], v[58:59], v[74:75]
	v_pk_fma_f32 v[76:77], v[12:13], v[60:61], v[76:77]
	v_pk_mul_f32 v[78:79], v[18:19], v[50:51]
	v_pk_mul_f32 v[80:81], v[20:21], v[52:53]
	v_pk_mul_f32 v[82:83], v[22:23], v[54:55]
	v_pk_mul_f32 v[84:85], v[24:25], v[56:57]
	v_pk_mul_f32 v[86:87], v[26:27], v[58:59]
	v_pk_mul_f32 v[88:89], v[28:29], v[60:61]
	v_rcp_f32_e32 v78, v78
	v_rcp_f32_e32 v79, v79
	v_rcp_f32_e32 v80, v80
	v_rcp_f32_e32 v81, v81
	v_rcp_f32_e32 v82, v82
	v_rcp_f32_e32 v83, v83
	v_rcp_f32_e32 v84, v84
	v_rcp_f32_e32 v85, v85
	v_rcp_f32_e32 v86, v86
	v_rcp_f32_e32 v87, v87
	v_rcp_f32_e32 v88, v88
	v_rcp_f32_e32 v89, v89
	v_pk_fma_f32 v[90:91], v[66:67], v[78:79], v[90:91]
	v_pk_fma_f32 v[92:93], v[68:69], v[80:81], v[92:93]
	v_pk_fma_f32 v[94:95], v[70:71], v[82:83], v[94:95]
	v_pk_fma_f32 v[96:97], v[72:73], v[84:85], v[96:97]
	v_pk_fma_f32 v[98:99], v[74:75], v[86:87], v[98:99]
	v_pk_fma_f32 v[100:101], v[76:77], v[88:89], v[100:101]
	v_fma_f32 v66, v90, -2.0, s28
	v_subrev_f32_e32 v66, s29, v66
	v_mul_f32_e32 v66, 0x3fb8aa3b, v66
	v_exp_f32_e32 v66, v66
	v_fma_f32 v67, v91, -2.0, s28
	v_subrev_f32_e32 v67, s29, v67
	v_mul_f32_e32 v67, 0x3fb8aa3b, v67
	v_exp_f32_e32 v67, v67
	v_fma_f32 v68, v92, -2.0, s28
	v_subrev_f32_e32 v68, s29, v68
	v_mul_f32_e32 v68, 0x3fb8aa3b, v68
	v_exp_f32_e32 v68, v68
	v_fma_f32 v69, v93, -2.0, s28
	v_subrev_f32_e32 v69, s29, v69
	v_mul_f32_e32 v69, 0x3fb8aa3b, v69
	v_exp_f32_e32 v69, v69
	v_fma_f32 v70, v94, -2.0, s28
	v_subrev_f32_e32 v70, s29, v70
	v_mul_f32_e32 v70, 0x3fb8aa3b, v70
	v_exp_f32_e32 v70, v70
	v_fma_f32 v71, v95, -2.0, s28
	v_subrev_f32_e32 v71, s29, v71
	v_mul_f32_e32 v71, 0x3fb8aa3b, v71
	v_exp_f32_e32 v71, v71
	v_fma_f32 v72, v96, -2.0, s28
	v_subrev_f32_e32 v72, s29, v72
	v_mul_f32_e32 v72, 0x3fb8aa3b, v72
	v_exp_f32_e32 v72, v72
	v_fma_f32 v73, v97, -2.0, s28
	v_subrev_f32_e32 v73, s29, v73
	v_mul_f32_e32 v73, 0x3fb8aa3b, v73
	v_exp_f32_e32 v73, v73
	v_fma_f32 v74, v98, -2.0, s28
	v_subrev_f32_e32 v74, s29, v74
	v_mul_f32_e32 v74, 0x3fb8aa3b, v74
	v_exp_f32_e32 v74, v74
	v_fma_f32 v75, v99, -2.0, s28
	v_subrev_f32_e32 v75, s29, v75
	v_mul_f32_e32 v75, 0x3fb8aa3b, v75
	v_exp_f32_e32 v75, v75
	v_fma_f32 v76, v100, -2.0, s28
	v_subrev_f32_e32 v76, s29, v76
	v_mul_f32_e32 v76, 0x3fb8aa3b, v76
	v_exp_f32_e32 v76, v76
	v_fma_f32 v77, v101, -2.0, s28
	v_subrev_f32_e32 v77, s29, v77
	v_mul_f32_e32 v77, 0x3fb8aa3b, v77
	v_exp_f32_e32 v77, v77
	s_nop 0
	v_cvt_f16_f32_e32 v66, v66
	v_cvt_f16_f32_e32 v67, v67
	v_cvt_f16_f32_e32 v68, v68
	v_cvt_f16_f32_e32 v69, v69
	v_cvt_f16_f32_e32 v70, v70
	v_cvt_f16_f32_e32 v71, v71
	v_cvt_f16_f32_e32 v72, v72
	v_cvt_f16_f32_e32 v73, v73
	v_cvt_f16_f32_e32 v74, v74
	v_cvt_f16_f32_e32 v75, v75
	v_cvt_f16_f32_e32 v76, v76
	v_cvt_f16_f32_e32 v77, v77
	ds_write_b16 v1, v66
	ds_write_b16 v1, v67 offset:800
	ds_write_b16 v1, v68 offset:1600
	ds_write_b16 v1, v69 offset:2400
	ds_write_b16 v1, v70 offset:6400
	ds_write_b16 v1, v71 offset:7200
	ds_write_b16 v1, v72 offset:8000
	ds_write_b16 v1, v73 offset:8800
	ds_write_b16 v1, v74 offset:12800
	ds_write_b16 v1, v75 offset:13600
	ds_write_b16 v1, v76 offset:14400
	ds_write_b16 v1, v77 offset:15200
	s_cmpk_gt_u32 s49, 0xff
	s_cbranch_scc1 .Lf_wo_done
	s_waitcnt vmcnt(0)
	v_cvt_f16_f32_e32 v2, v102
	v_cvt_f16_f32_e32 v5, v105
	v_cvt_pk_f16_f32 v3, v103, v104
	v_pack_b32_f16 v2, v2, v3
	v_alignbit_b32 v3, v5, v3, 16
	v_and_b32_e32 v6, 0xff, v0
	v_lshlrev_b32_e32 v6, 3, v6
	s_lshl_b32 s22, s42, 1
	v_add_u32_e32 v6, s22, v6
	global_store_dwordx2 v6, v[2:3], s[18:19]
